# v16: + accumulator zeroing with 64-bit moves
# speedup vs baseline: 1.0037x; 1.0037x over previous
; template <bool GATHER, bool F8, class Epi, class Sched>
; __device__ __forceinline__ void gemm_phase(LAS unsigned char* lds, const int nt, const unsigned lda, const unsigned ldb, const Sched& S, const Epi& E) {
;     ...
;         if (!cur.keep) {
; #pragma unroll
;             for (int a = 0; a < 2; ++a)
; #pragma unroll
;                 for (int b = 0; b < 2; ++b)
; #pragma unroll
;                     for (int m = 0; m < 4; ++m)
; #pragma unroll
;                         for (int n = 0; n < 2; ++n) acc[a][b][m][n] = (f32x4){0.f, 0.f, 0.f, 0.f};
;         }
.LBB0_386:
	s_add_u32 s24, s24, 0x40080
	s_addc_u32 s25, s25, 0
	s_add_u32 s30, s26, 0x100
	v_mov_b32_e32 v34, 0
	s_addc_u32 s54, s27, 0
	s_mov_b32 s55, -2
	v_mov_b32_e32 v35, v34
	v_mov_b64_e32 v[36:37], v[34:35]
	v_mov_b64_e32 v[38:39], v[34:35]
	v_mov_b64_e32 v[40:41], v[34:35]
	v_mov_b64_e32 v[42:43], v[34:35]
	v_mov_b64_e32 v[44:45], v[34:35]
	v_mov_b64_e32 v[46:47], v[34:35]
	v_mov_b64_e32 v[48:49], v[34:35]
	v_mov_b64_e32 v[50:51], v[34:35]
	v_mov_b64_e32 v[52:53], v[34:35]
	v_mov_b64_e32 v[54:55], v[34:35]
	v_mov_b64_e32 v[56:57], v[34:35]
	v_mov_b64_e32 v[58:59], v[34:35]
	v_mov_b64_e32 v[60:61], v[34:35]
	v_mov_b64_e32 v[62:63], v[34:35]
	v_mov_b64_e32 v[64:65], v[34:35]
	v_mov_b64_e32 v[66:67], v[34:35]
	v_mov_b64_e32 v[68:69], v[34:35]
	v_mov_b64_e32 v[70:71], v[34:35]
	v_mov_b64_e32 v[72:73], v[34:35]
	v_mov_b64_e32 v[74:75], v[34:35]
	v_mov_b64_e32 v[76:77], v[34:35]
	v_mov_b64_e32 v[78:79], v[34:35]
	v_mov_b64_e32 v[80:81], v[34:35]
	v_mov_b64_e32 v[82:83], v[34:35]
	v_mov_b64_e32 v[84:85], v[34:35]
	v_mov_b64_e32 v[86:87], v[34:35]
	v_mov_b64_e32 v[88:89], v[34:35]
	v_mov_b64_e32 v[90:91], v[34:35]
	v_mov_b64_e32 v[92:93], v[34:35]
	v_mov_b64_e32 v[94:95], v[34:35]
	v_mov_b64_e32 v[96:97], v[34:35]
	v_mov_b64_e32 v[98:99], v[34:35]
	v_mov_b64_e32 v[100:101], v[34:35]
	v_mov_b64_e32 v[102:103], v[34:35]
	v_mov_b64_e32 v[104:105], v[34:35]
	v_mov_b64_e32 v[106:107], v[34:35]
	v_mov_b64_e32 v[108:109], v[34:35]
	v_mov_b64_e32 v[110:111], v[34:35]
	v_mov_b64_e32 v[112:113], v[34:35]
	v_mov_b64_e32 v[114:115], v[34:35]
	v_mov_b64_e32 v[116:117], v[34:35]
	v_mov_b64_e32 v[118:119], v[34:35]
	v_mov_b64_e32 v[120:121], v[34:35]
	v_mov_b64_e32 v[122:123], v[34:35]
	v_mov_b64_e32 v[124:125], v[34:35]
	v_mov_b64_e32 v[126:127], v[34:35]
	v_mov_b64_e32 v[128:129], v[34:35]
	v_mov_b64_e32 v[130:131], v[34:35]
	v_mov_b64_e32 v[132:133], v[34:35]
	v_mov_b64_e32 v[134:135], v[34:35]
	v_mov_b64_e32 v[136:137], v[34:35]
	v_mov_b64_e32 v[138:139], v[34:35]
	v_mov_b64_e32 v[140:141], v[34:35]
	v_mov_b64_e32 v[142:143], v[34:35]
	v_mov_b64_e32 v[144:145], v[34:35]
	v_mov_b64_e32 v[146:147], v[34:35]
	v_mov_b64_e32 v[148:149], v[34:35]
	v_mov_b64_e32 v[150:151], v[34:35]
	v_mov_b64_e32 v[152:153], v[34:35]
	v_mov_b64_e32 v[154:155], v[34:35]
	v_mov_b64_e32 v[156:157], v[34:35]
	v_mov_b64_e32 v[158:159], v[34:35]
	v_mov_b64_e32 v[160:161], v[34:35]

; template <class TIn, class TOut, int QS, int KS, int OS, bool BIAS, bool PREF = true>
; __device__ __forceinline__ void causal_swa_block(const BlockRef<TIn, TOut>& cur, const BlockRef<TIn, TOut>& nxt, int skv, int W, char* lds, Seam<TIn>& S) {
;     ...
;     float m_reg = BIAS ? ((const float*)(lds + BIAS_OFF))[cur.P0 + wid * QBLK + r32] : -1e30f, l_reg = 0; f32x16 o[4] = {};
.LBB0_492:
	v_mov_b32_e32 v66, 0
	v_mov_b32_e32 v67, v66
	v_mov_b64_e32 v[2:3], v[66:67]
	v_mov_b64_e32 v[4:5], v[66:67]
	v_mov_b64_e32 v[6:7], v[66:67]
	v_mov_b64_e32 v[8:9], v[66:67]
	v_mov_b64_e32 v[10:11], v[66:67]
	v_mov_b64_e32 v[12:13], v[66:67]
	v_mov_b64_e32 v[14:15], v[66:67]
	v_mov_b64_e32 v[16:17], v[66:67]
	v_mov_b64_e32 v[18:19], v[66:67]
	v_mov_b64_e32 v[20:21], v[66:67]
	v_mov_b64_e32 v[22:23], v[66:67]
	v_mov_b64_e32 v[24:25], v[66:67]
	v_mov_b64_e32 v[26:27], v[66:67]
	v_mov_b64_e32 v[28:29], v[66:67]
	v_mov_b64_e32 v[30:31], v[66:67]
	v_mov_b64_e32 v[32:33], v[66:67]
	v_mov_b64_e32 v[34:35], v[66:67]
	v_mov_b64_e32 v[36:37], v[66:67]
	v_mov_b64_e32 v[38:39], v[66:67]
	v_mov_b64_e32 v[40:41], v[66:67]
	v_mov_b64_e32 v[42:43], v[66:67]
	v_mov_b64_e32 v[44:45], v[66:67]
	v_mov_b64_e32 v[46:47], v[66:67]
	v_mov_b64_e32 v[48:49], v[66:67]
	v_mov_b64_e32 v[50:51], v[66:67]
	v_mov_b64_e32 v[52:53], v[66:67]
	v_mov_b64_e32 v[54:55], v[66:67]
	v_mov_b64_e32 v[56:57], v[66:67]
	v_mov_b64_e32 v[58:59], v[66:67]
	v_mov_b64_e32 v[60:61], v[66:67]
	v_mov_b64_e32 v[62:63], v[66:67]
	v_mov_b64_e32 v[64:65], v[66:67]
	v_mov_b64_e32 v[68:69], v[66:67]
	v_mov_b64_e32 v[70:71], v[66:67]
	v_mov_b64_e32 v[72:73], v[66:67]
	v_mov_b64_e32 v[74:75], v[66:67]
	v_mov_b64_e32 v[76:77], v[66:67]
	v_mov_b64_e32 v[78:79], v[66:67]
	v_mov_b64_e32 v[80:81], v[66:67]
	v_mov_b32_e32 v224, v66

; template <class TIn, class TOut, int QS, int KS, int OS, bool BIAS, bool PREF = true>
; __device__ __forceinline__ void causal_swa_block(const BlockRef<TIn, TOut>& cur, const BlockRef<TIn, TOut>& nxt, int skv, int W, char* lds, Seam<TIn>& S) {
;     ...
;     float m_reg = BIAS ? ((const float*)(lds + BIAS_OFF))[cur.P0 + wid * QBLK + r32] : -1e30f, l_reg = 0; f32x16 o[4] = {};
.LBB0_658:
	v_mov_b32_e32 v66, 0
	v_mov_b32_e32 v67, v66
	v_mov_b64_e32 v[2:3], v[66:67]
	v_mov_b64_e32 v[4:5], v[66:67]
	v_mov_b64_e32 v[6:7], v[66:67]
	v_mov_b64_e32 v[8:9], v[66:67]
	v_mov_b64_e32 v[10:11], v[66:67]
	v_mov_b64_e32 v[12:13], v[66:67]
	v_mov_b64_e32 v[14:15], v[66:67]
	v_mov_b64_e32 v[16:17], v[66:67]
	v_mov_b64_e32 v[18:19], v[66:67]
	v_mov_b64_e32 v[20:21], v[66:67]
	v_mov_b64_e32 v[22:23], v[66:67]
	v_mov_b64_e32 v[24:25], v[66:67]
	v_mov_b64_e32 v[26:27], v[66:67]
	v_mov_b64_e32 v[28:29], v[66:67]
	v_mov_b64_e32 v[30:31], v[66:67]
	v_mov_b64_e32 v[32:33], v[66:67]
	v_mov_b64_e32 v[34:35], v[66:67]
	v_mov_b64_e32 v[36:37], v[66:67]
	v_mov_b64_e32 v[38:39], v[66:67]
	v_mov_b64_e32 v[40:41], v[66:67]
	v_mov_b64_e32 v[42:43], v[66:67]
	v_mov_b64_e32 v[44:45], v[66:67]
	v_mov_b64_e32 v[46:47], v[66:67]
	v_mov_b64_e32 v[48:49], v[66:67]
	v_mov_b64_e32 v[50:51], v[66:67]
	v_mov_b64_e32 v[52:53], v[66:67]
	v_mov_b64_e32 v[54:55], v[66:67]
	v_mov_b64_e32 v[56:57], v[66:67]
	v_mov_b64_e32 v[58:59], v[66:67]
	v_mov_b64_e32 v[60:61], v[66:67]
	v_mov_b64_e32 v[62:63], v[66:67]
	v_mov_b64_e32 v[64:65], v[66:67]
	v_mov_b64_e32 v[68:69], v[66:67]
	v_mov_b64_e32 v[70:71], v[66:67]
	v_mov_b64_e32 v[72:73], v[66:67]
	v_mov_b64_e32 v[74:75], v[66:67]
	v_mov_b64_e32 v[76:77], v[66:67]
	v_mov_b64_e32 v[78:79], v[66:67]
	v_mov_b64_e32 v[80:81], v[66:67]
	v_mov_b32_e32 v216, v66

; template <bool GATHER, bool F8, class Epi, class Sched>
; __device__ __forceinline__ void gemm_phase(LAS unsigned char* lds, const int nt, const unsigned lda, const unsigned ldb, const Sched& S, const Epi& E) {
;     ...
;         if (!cur.keep) {
; #pragma unroll
;             for (int a = 0; a < 2; ++a)
; #pragma unroll
;                 for (int b = 0; b < 2; ++b)
; #pragma unroll
;                     for (int m = 0; m < 4; ++m)
; #pragma unroll
;                         for (int n = 0; n < 2; ++n) acc[a][b][m][n] = (f32x4){0.f, 0.f, 0.f, 0.f};
;         }
.LBB0_1033:
	s_add_u32 s22, s22, 0x80080
	s_addc_u32 s23, s23, 0
	s_add_u32 s21, s24, 0x100
	v_mov_b32_e32 v2, 0
	s_addc_u32 s28, s25, 0
	s_mov_b32 s48, -2
	s_waitcnt lgkmcnt(0)
	v_mov_b32_e32 v3, v2
	v_mov_b64_e32 v[4:5], v[2:3]
	v_mov_b64_e32 v[6:7], v[2:3]
	v_mov_b64_e32 v[8:9], v[2:3]
	v_mov_b64_e32 v[10:11], v[2:3]
	v_mov_b64_e32 v[12:13], v[2:3]
	v_mov_b64_e32 v[14:15], v[2:3]
	v_mov_b64_e32 v[16:17], v[2:3]
	v_mov_b64_e32 v[18:19], v[2:3]
	v_mov_b64_e32 v[20:21], v[2:3]
	v_mov_b64_e32 v[22:23], v[2:3]
	v_mov_b64_e32 v[24:25], v[2:3]
	v_mov_b64_e32 v[26:27], v[2:3]
	v_mov_b64_e32 v[28:29], v[2:3]
	v_mov_b64_e32 v[30:31], v[2:3]
	v_mov_b64_e32 v[32:33], v[2:3]
	v_mov_b64_e32 v[34:35], v[2:3]
	v_mov_b64_e32 v[36:37], v[2:3]
	v_mov_b64_e32 v[38:39], v[2:3]
	v_mov_b64_e32 v[40:41], v[2:3]
	v_mov_b64_e32 v[42:43], v[2:3]
	v_mov_b64_e32 v[44:45], v[2:3]
	v_mov_b64_e32 v[46:47], v[2:3]
	v_mov_b64_e32 v[48:49], v[2:3]
	v_mov_b64_e32 v[50:51], v[2:3]
	v_mov_b64_e32 v[52:53], v[2:3]
	v_mov_b64_e32 v[54:55], v[2:3]
	v_mov_b64_e32 v[56:57], v[2:3]
	v_mov_b64_e32 v[58:59], v[2:3]
	v_mov_b64_e32 v[60:61], v[2:3]
	v_mov_b64_e32 v[62:63], v[2:3]
	v_mov_b64_e32 v[64:65], v[2:3]
	v_mov_b64_e32 v[66:67], v[2:3]
	v_mov_b64_e32 v[68:69], v[2:3]
	v_mov_b64_e32 v[70:71], v[2:3]
	v_mov_b64_e32 v[72:73], v[2:3]
	v_mov_b64_e32 v[74:75], v[2:3]
	v_mov_b64_e32 v[76:77], v[2:3]
	v_mov_b64_e32 v[78:79], v[2:3]
	v_mov_b64_e32 v[80:81], v[2:3]
	v_mov_b64_e32 v[82:83], v[2:3]
	v_mov_b64_e32 v[84:85], v[2:3]
	v_mov_b64_e32 v[86:87], v[2:3]
	v_mov_b64_e32 v[88:89], v[2:3]
	v_mov_b64_e32 v[90:91], v[2:3]
	v_mov_b64_e32 v[92:93], v[2:3]
	v_mov_b64_e32 v[94:95], v[2:3]
	v_mov_b64_e32 v[96:97], v[2:3]
	v_mov_b64_e32 v[98:99], v[2:3]
	v_mov_b64_e32 v[100:101], v[2:3]
	v_mov_b64_e32 v[102:103], v[2:3]
	v_mov_b64_e32 v[104:105], v[2:3]
	v_mov_b64_e32 v[106:107], v[2:3]
	v_mov_b64_e32 v[108:109], v[2:3]
	v_mov_b64_e32 v[110:111], v[2:3]
	v_mov_b64_e32 v[112:113], v[2:3]
	v_mov_b64_e32 v[114:115], v[2:3]
	v_mov_b64_e32 v[116:117], v[2:3]
	v_mov_b64_e32 v[118:119], v[2:3]
	v_mov_b64_e32 v[120:121], v[2:3]
	v_mov_b64_e32 v[122:123], v[2:3]
	v_mov_b64_e32 v[124:125], v[2:3]
	v_mov_b64_e32 v[126:127], v[2:3]
	v_mov_b64_e32 v[128:129], v[2:3]

; template <bool GATHER, bool F8, class Epi, class Sched>
; __device__ __forceinline__ void gemm_phase(LAS unsigned char* lds, const int nt, const unsigned lda, const unsigned ldb, const Sched& S, const Epi& E) {
;     ...
;         if (!cur.keep) {
; #pragma unroll
;             for (int a = 0; a < 2; ++a)
; #pragma unroll
;                 for (int b = 0; b < 2; ++b)
; #pragma unroll
;                     for (int m = 0; m < 4; ++m)
; #pragma unroll
;                         for (int n = 0; n < 2; ++n) acc[a][b][m][n] = (f32x4){0.f, 0.f, 0.f, 0.f};
;         }
.LBB0_1431:
	s_add_u32 s26, s26, 0x20080
	s_addc_u32 s27, s27, 0
	s_add_u32 s25, s28, 0x100
	v_mov_b32_e32 v2, 0
	s_addc_u32 s34, s29, 0
	s_mov_b32 s53, -2
	s_waitcnt lgkmcnt(0)
	v_mov_b32_e32 v3, v2
	v_mov_b64_e32 v[4:5], v[2:3]
	v_mov_b64_e32 v[6:7], v[2:3]
	v_mov_b64_e32 v[8:9], v[2:3]
	v_mov_b64_e32 v[10:11], v[2:3]
	v_mov_b64_e32 v[12:13], v[2:3]
	v_mov_b64_e32 v[14:15], v[2:3]
	v_mov_b64_e32 v[16:17], v[2:3]
	v_mov_b64_e32 v[18:19], v[2:3]
	v_mov_b64_e32 v[20:21], v[2:3]
	v_mov_b64_e32 v[22:23], v[2:3]
	v_mov_b64_e32 v[24:25], v[2:3]
	v_mov_b64_e32 v[26:27], v[2:3]
	v_mov_b64_e32 v[28:29], v[2:3]
	v_mov_b64_e32 v[30:31], v[2:3]
	v_mov_b64_e32 v[32:33], v[2:3]
	v_mov_b64_e32 v[34:35], v[2:3]
	v_mov_b64_e32 v[36:37], v[2:3]
	v_mov_b64_e32 v[38:39], v[2:3]
	v_mov_b64_e32 v[40:41], v[2:3]
	v_mov_b64_e32 v[42:43], v[2:3]
	v_mov_b64_e32 v[44:45], v[2:3]
	v_mov_b64_e32 v[46:47], v[2:3]
	v_mov_b64_e32 v[48:49], v[2:3]
	v_mov_b64_e32 v[50:51], v[2:3]
	v_mov_b64_e32 v[52:53], v[2:3]
	v_mov_b64_e32 v[54:55], v[2:3]
	v_mov_b64_e32 v[56:57], v[2:3]
	v_mov_b64_e32 v[58:59], v[2:3]
	v_mov_b64_e32 v[60:61], v[2:3]
	v_mov_b64_e32 v[62:63], v[2:3]
	v_mov_b64_e32 v[64:65], v[2:3]
	v_mov_b64_e32 v[66:67], v[2:3]
	v_mov_b64_e32 v[68:69], v[2:3]
	v_mov_b64_e32 v[70:71], v[2:3]
	v_mov_b64_e32 v[72:73], v[2:3]
	v_mov_b64_e32 v[74:75], v[2:3]
	v_mov_b64_e32 v[76:77], v[2:3]
	v_mov_b64_e32 v[78:79], v[2:3]
	v_mov_b64_e32 v[80:81], v[2:3]
	v_mov_b64_e32 v[82:83], v[2:3]
	v_mov_b64_e32 v[84:85], v[2:3]
	v_mov_b64_e32 v[86:87], v[2:3]
	v_mov_b64_e32 v[88:89], v[2:3]
	v_mov_b64_e32 v[90:91], v[2:3]
	v_mov_b64_e32 v[92:93], v[2:3]
	v_mov_b64_e32 v[94:95], v[2:3]
	v_mov_b64_e32 v[96:97], v[2:3]
	v_mov_b64_e32 v[98:99], v[2:3]
	v_mov_b64_e32 v[100:101], v[2:3]
	v_mov_b64_e32 v[102:103], v[2:3]
	v_mov_b64_e32 v[104:105], v[2:3]
	v_mov_b64_e32 v[106:107], v[2:3]
	v_mov_b64_e32 v[108:109], v[2:3]
	v_mov_b64_e32 v[110:111], v[2:3]
	v_mov_b64_e32 v[112:113], v[2:3]
	v_mov_b64_e32 v[114:115], v[2:3]
	v_mov_b64_e32 v[116:117], v[2:3]
	v_mov_b64_e32 v[118:119], v[2:3]
	v_mov_b64_e32 v[120:121], v[2:3]
	v_mov_b64_e32 v[122:123], v[2:3]
	v_mov_b64_e32 v[124:125], v[2:3]
	v_mov_b64_e32 v[126:127], v[2:3]
	v_mov_b64_e32 v[128:129], v[2:3]

; template <bool GATHER, bool F8, class Epi, class Sched>
; __device__ __forceinline__ void gemm_phase(LAS unsigned char* lds, const int nt, const unsigned lda, const unsigned ldb, const Sched& S, const Epi& E) {
;     ...
;         if (!cur.keep) {
; #pragma unroll
;             for (int a = 0; a < 2; ++a)
; #pragma unroll
;                 for (int b = 0; b < 2; ++b)
; #pragma unroll
;                     for (int m = 0; m < 4; ++m)
; #pragma unroll
;                         for (int n = 0; n < 2; ++n) acc[a][b][m][n] = (f32x4){0.f, 0.f, 0.f, 0.f};
;         }
.LBB0_1926:
	s_add_u32 s0, s28, 0x80
	s_addc_u32 s1, s29, 0
	v_mov_b32_e32 v173, v165
	v_mov_b32_e32 v175, v165
	s_add_u32 s7, s34, 0x100
	v_mov_b32_e32 v62, 0
	v_lshl_add_u64 v[176:177], s[0:1], 0, v[174:175]
	v_lshl_add_u64 v[178:179], s[0:1], 0, v[172:173]
	s_addc_u32 s38, s35, 0
	s_mov_b32 s39, -2
	s_mov_b64 s[0:1], 0
	v_mov_b32_e32 v63, v62
	v_mov_b64_e32 v[34:35], v[62:63]
	v_mov_b64_e32 v[36:37], v[62:63]
	v_mov_b64_e32 v[38:39], v[62:63]
	v_mov_b64_e32 v[40:41], v[62:63]
	v_mov_b64_e32 v[42:43], v[62:63]
	v_mov_b64_e32 v[44:45], v[62:63]
	v_mov_b64_e32 v[46:47], v[62:63]
	v_mov_b64_e32 v[48:49], v[62:63]
	v_mov_b64_e32 v[50:51], v[62:63]
	v_mov_b64_e32 v[52:53], v[62:63]
	v_mov_b64_e32 v[54:55], v[62:63]
	v_mov_b64_e32 v[56:57], v[62:63]
	v_mov_b64_e32 v[58:59], v[62:63]
	v_mov_b64_e32 v[60:61], v[62:63]
	v_mov_b64_e32 v[64:65], v[62:63]
	v_mov_b64_e32 v[66:67], v[62:63]
	v_mov_b64_e32 v[68:69], v[62:63]
	v_mov_b64_e32 v[70:71], v[62:63]
	v_mov_b64_e32 v[72:73], v[62:63]
	v_mov_b64_e32 v[74:75], v[62:63]
	v_mov_b64_e32 v[76:77], v[62:63]
	v_mov_b64_e32 v[78:79], v[62:63]
	v_mov_b64_e32 v[80:81], v[62:63]
	v_mov_b64_e32 v[82:83], v[62:63]
	v_mov_b64_e32 v[84:85], v[62:63]
	v_mov_b64_e32 v[86:87], v[62:63]
	v_mov_b64_e32 v[88:89], v[62:63]
	v_mov_b64_e32 v[90:91], v[62:63]
	v_mov_b64_e32 v[92:93], v[62:63]
	v_mov_b64_e32 v[94:95], v[62:63]
	v_mov_b64_e32 v[96:97], v[62:63]
	v_mov_b64_e32 v[98:99], v[62:63]
	v_mov_b64_e32 v[100:101], v[62:63]
	v_mov_b64_e32 v[102:103], v[62:63]
	v_mov_b64_e32 v[104:105], v[62:63]
	v_mov_b64_e32 v[106:107], v[62:63]
	v_mov_b64_e32 v[108:109], v[62:63]
	v_mov_b64_e32 v[110:111], v[62:63]
	v_mov_b64_e32 v[112:113], v[62:63]
	v_mov_b64_e32 v[114:115], v[62:63]
	v_mov_b64_e32 v[116:117], v[62:63]
	v_mov_b64_e32 v[118:119], v[62:63]
	v_mov_b64_e32 v[120:121], v[62:63]
	v_mov_b64_e32 v[122:123], v[62:63]
	v_mov_b64_e32 v[124:125], v[62:63]
	v_mov_b64_e32 v[126:127], v[62:63]
	v_mov_b64_e32 v[128:129], v[62:63]
	v_mov_b64_e32 v[130:131], v[62:63]
	v_mov_b64_e32 v[132:133], v[62:63]
	v_mov_b64_e32 v[134:135], v[62:63]
	v_mov_b64_e32 v[136:137], v[62:63]
	v_mov_b64_e32 v[138:139], v[62:63]
	v_mov_b64_e32 v[140:141], v[62:63]
	v_mov_b64_e32 v[142:143], v[62:63]
	v_mov_b64_e32 v[144:145], v[62:63]
	v_mov_b64_e32 v[146:147], v[62:63]
	v_mov_b64_e32 v[148:149], v[62:63]
	v_mov_b64_e32 v[150:151], v[62:63]
	v_mov_b64_e32 v[152:153], v[62:63]
	v_mov_b64_e32 v[154:155], v[62:63]
	v_mov_b64_e32 v[156:157], v[62:63]
	v_mov_b64_e32 v[158:159], v[62:63]
	v_mov_b64_e32 v[160:161], v[62:63]

; template <bool GATHER, bool F8, class Epi, class Sched>
; __device__ __forceinline__ void gemm_phase(LAS unsigned char* lds, const int nt, const unsigned lda, const unsigned ldb, const Sched& S, const Epi& E) {
;     ...
;         if (!cur.keep) {
; #pragma unroll
;             for (int a = 0; a < 2; ++a)
; #pragma unroll
;                 for (int b = 0; b < 2; ++b)
; #pragma unroll
;                     for (int m = 0; m < 4; ++m)
; #pragma unroll
;                         for (int n = 0; n < 2; ++n) acc[a][b][m][n] = (f32x4){0.f, 0.f, 0.f, 0.f};
;         }
.LBB0_2017:
	s_add_u32 s26, s26, 0x40080
	s_addc_u32 s27, s27, 0
	s_add_u32 s7, s28, 0x100
	v_mov_b32_e32 v34, 0
	s_addc_u32 s12, s29, 0
	s_mov_b32 s58, -2
	v_mov_b32_e32 v35, v34
	v_mov_b64_e32 v[36:37], v[34:35]
	v_mov_b64_e32 v[38:39], v[34:35]
	v_mov_b64_e32 v[40:41], v[34:35]
	v_mov_b64_e32 v[42:43], v[34:35]
	v_mov_b64_e32 v[44:45], v[34:35]
	v_mov_b64_e32 v[46:47], v[34:35]
	v_mov_b64_e32 v[48:49], v[34:35]
	v_mov_b64_e32 v[50:51], v[34:35]
	v_mov_b64_e32 v[52:53], v[34:35]
	v_mov_b64_e32 v[54:55], v[34:35]
	v_mov_b64_e32 v[56:57], v[34:35]
	v_mov_b64_e32 v[58:59], v[34:35]
	v_mov_b64_e32 v[60:61], v[34:35]
	v_mov_b64_e32 v[62:63], v[34:35]
	v_mov_b64_e32 v[64:65], v[34:35]
	v_mov_b64_e32 v[66:67], v[34:35]
	v_mov_b64_e32 v[68:69], v[34:35]
	v_mov_b64_e32 v[70:71], v[34:35]
	v_mov_b64_e32 v[72:73], v[34:35]
	v_mov_b64_e32 v[74:75], v[34:35]
	v_mov_b64_e32 v[76:77], v[34:35]
	v_mov_b64_e32 v[78:79], v[34:35]
	v_mov_b64_e32 v[80:81], v[34:35]
	v_mov_b64_e32 v[82:83], v[34:35]
	v_mov_b64_e32 v[84:85], v[34:35]
	v_mov_b64_e32 v[86:87], v[34:35]
	v_mov_b64_e32 v[88:89], v[34:35]
	v_mov_b64_e32 v[90:91], v[34:35]
	v_mov_b64_e32 v[92:93], v[34:35]
	v_mov_b64_e32 v[94:95], v[34:35]
	v_mov_b64_e32 v[96:97], v[34:35]
	v_mov_b64_e32 v[98:99], v[34:35]
	v_mov_b64_e32 v[100:101], v[34:35]
	v_mov_b64_e32 v[102:103], v[34:35]
	v_mov_b64_e32 v[104:105], v[34:35]
	v_mov_b64_e32 v[106:107], v[34:35]
	v_mov_b64_e32 v[108:109], v[34:35]
	v_mov_b64_e32 v[110:111], v[34:35]
	v_mov_b64_e32 v[112:113], v[34:35]
	v_mov_b64_e32 v[114:115], v[34:35]
	v_mov_b64_e32 v[116:117], v[34:35]
	v_mov_b64_e32 v[118:119], v[34:35]
	v_mov_b64_e32 v[120:121], v[34:35]
	v_mov_b64_e32 v[122:123], v[34:35]
	v_mov_b64_e32 v[124:125], v[34:35]
	v_mov_b64_e32 v[126:127], v[34:35]
	v_mov_b64_e32 v[128:129], v[34:35]
	v_mov_b64_e32 v[130:131], v[34:35]
	v_mov_b64_e32 v[132:133], v[34:35]
	v_mov_b64_e32 v[134:135], v[34:35]
	v_mov_b64_e32 v[136:137], v[34:35]
	v_mov_b64_e32 v[138:139], v[34:35]
	v_mov_b64_e32 v[140:141], v[34:35]
	v_mov_b64_e32 v[142:143], v[34:35]
	v_mov_b64_e32 v[144:145], v[34:35]
	v_mov_b64_e32 v[146:147], v[34:35]
	v_mov_b64_e32 v[148:149], v[34:35]
	v_mov_b64_e32 v[150:151], v[34:35]
	v_mov_b64_e32 v[152:153], v[34:35]
	v_mov_b64_e32 v[154:155], v[34:35]
	v_mov_b64_e32 v[156:157], v[34:35]
	v_mov_b64_e32 v[158:159], v[34:35]
	v_mov_b64_e32 v[160:161], v[34:35]
